# v3 + P9 attention sink from a lane table in v255 via v_readlane instead of a per-item global load; its vmcnt(0) removed
# baseline (speedup 1.0000x reference)
.LBB0_834:
	s_cmp_lt_i32 s96, 10
	s_cselect_b64 s[2:3], -1, 0
	s_and_b64 s[0:1], s[2:3], s[0:1]
	s_andn2_b64 vcc, exec, s[0:1]
	s_cbranch_vccnz .LBB0_887
	v_mbcnt_hi_u32_b32 v10, -1, v248
	v_add_u32_e32 v0, s84, v10
	v_and_b32_e32 v1, 15, v10
	v_lshlrev_b32_e32 v1, 2, v1
	global_load_dword v2, v1, s[70:71]
	s_mov_b64 s[2:3], exec
	s_waitcnt vmcnt(0)
	s_mov_b64 exec, 0xffff0000
	v_mov_b32_e32 v255, v2
	s_mov_b64 exec, s[2:3]
	s_movk_i32 s2, 0x800
	s_nop 0
	v_readfirstlane_b32 s23, v0
	v_cmp_gt_i32_e32 vcc, s2, v0
	s_and_saveexec_b64 s[4:5], vcc
	s_cbranch_execz .LBB0_848
	s_waitcnt lgkmcnt(0)
	v_and_b32_e32 v1, 0x7f, v0
	v_cvt_f32_ubyte0_e32 v2, v1
	v_mul_f32_e32 v2, 0x3d800000, v2
	s_mov_b32 s2, 0x800000
	v_cmp_gt_f32_e32 vcc, s2, v2
	s_mov_b32 s2, 0x3f317217
	s_mov_b32 s6, 0x40051592
	v_cndmask_b32_e64 v3, 0, 32, vcc
	v_ldexp_f32 v2, v2, v3
	v_log_f32_e32 v2, v2
	s_nop 0
	v_mul_f32_e32 v3, 0x3f317217, v2
	v_fma_f32 v3, v2, s2, -v3
	v_fmamk_f32 v3, v2, 0x3377d1cf, v3
	s_mov_b32 s2, 0x7f800000
	v_fmac_f32_e32 v3, 0x3f317217, v2
	v_cmp_lt_f32_e64 s[2:3], |v2|, s2
	s_nop 1
	v_cndmask_b32_e64 v2, v2, v3, s[2:3]
	v_mov_b32_e32 v3, 0x41b17218
	v_cndmask_b32_e32 v3, 0, v3, vcc
	v_sub_f32_e32 v2, v2, v3
	v_div_scale_f32 v3, s[2:3], s6, s6, v2
	v_rcp_f32_e32 v4, v3
	s_movk_i32 s2, 0x1ff
	v_fma_f32 v5, -v3, v4, 1.0
	v_fmac_f32_e32 v4, v5, v4
	v_div_scale_f32 v5, vcc, v2, s6, v2
	v_mul_f32_e32 v6, v5, v4
	v_fma_f32 v7, -v3, v6, v5
	v_fmac_f32_e32 v6, v7, v4
	v_fma_f32 v3, -v3, v6, v5
	v_div_fmas_f32 v3, v3, v4, v6
	v_div_fixup_f32 v2, v3, s6, v2
	v_mul_f32_e32 v2, 0x41800000, v2
	v_cvt_i32_f32_e32 v2, v2
	v_cmp_gt_u32_e32 vcc, 16, v1
	s_mov_b64 s[6:7], -1
	v_min_i32_e32 v2, 15, v2
	v_add_u32_e32 v2, 16, v2
	v_cndmask_b32_e32 v1, v2, v1, vcc
	v_lshlrev_b32_e32 v4, 4, v1
	v_max_i32_e32 v1, 0x600, v0
	v_sub_u32_e32 v1, v1, v0
	v_add_u32_e32 v2, 0x1ff, v1
	v_cmp_lt_u32_e32 vcc, s2, v2
	v_mov_b32_e32 v1, v0
	s_and_saveexec_b64 s[2:3], vcc
	s_cbranch_execz .LBB0_845
	v_lshrrev_b32_e32 v5, 9, v2
	v_add_u32_e32 v2, -1, v5
	v_add_u32_e32 v1, 0x200, v0
	v_lshrrev_b32_e32 v3, 1, v2
	v_add_u32_e32 v6, 1, v3
	v_cmp_lt_u32_e32 vcc, 5, v2
	v_mov_b32_e32 v9, 0
	v_mov_b64_e32 v[2:3], v[0:1]
	s_and_saveexec_b64 s[6:7], vcc
	s_cbranch_execz .LBB0_841
	v_lshl_add_u32 v2, v0, 2, 0
	v_and_b32_e32 v7, -4, v6
	s_mov_b32 s11, 0
	v_add_u32_e32 v8, 0x1a000, v2
	s_mov_b64 s[8:9], 0
	s_mov_b32 s10, 0x3fb8aa3b
	v_mov_b64_e32 v[2:3], v[0:1]

.LBB0_869:
	s_ashr_i32 s38, s37, 31
	s_lshr_b32 s2, s38, 25
	s_add_i32 s2, s37, s2
	s_ashr_i32 s39, s2, 7
	s_lshr_b32 s2, s39, 30
	s_add_i32 s2, s39, s2
	s_and_b32 s2, s2, 0x3ffffffc
	s_sub_i32 s2, s39, s2
	s_lshl_b32 s2, s2, 2
	s_or_b32 s8, s2, s22
	s_mul_i32 s2, s34, 0xd000
	s_ashr_i32 s9, s8, 31
	s_add_i32 s36, s2, 0
	s_add_i32 s35, s37, s72
	s_add_i32 s2, s8, 16
	s_nop 3
	v_readlane_b32 s3, v255, s2
	s_nop 1
	v_mov_b32_e32 v156, s3
	s_lshl_b32 s2, s8, 9
	s_add_i32 s2, s2, 0
	v_mov_b32_e32 v157, v123
	s_add_i32 s2, s2, 0x1a000
	v_add3_u32 v113, s36, v140, v144
	v_lshl_add_u32 v74, v157, 2, s2
	ds_read2_b32 v[2:3], v74 offset0:127 offset1:128
	ds_read2_b32 v[4:5], v74 offset0:125 offset1:126
	ds_read2_b32 v[6:7], v74 offset0:119 offset1:120
	ds_read2_b32 v[8:9], v74 offset0:117 offset1:118
	ds_read2_b32 v[10:11], v74 offset0:111 offset1:112
	ds_read2_b32 v[12:13], v74 offset0:109 offset1:110
	ds_read2_b32 v[14:15], v74 offset0:103 offset1:104
	ds_read2_b32 v[20:21], v74 offset0:101 offset1:102
	ds_read_b128 v[16:19], v113
	s_waitcnt lgkmcnt(8)
	v_mov_b32_e32 v0, v3
	v_mov_b32_e32 v1, v2
	s_waitcnt lgkmcnt(7)
	v_mov_b32_e32 v2, v5
	v_mov_b32_e32 v3, v4
	s_waitcnt lgkmcnt(6)
	v_mov_b32_e32 v4, v7
	v_mov_b32_e32 v5, v6
	s_waitcnt lgkmcnt(5)
	v_mov_b32_e32 v6, v9
	v_mov_b32_e32 v7, v8
	s_waitcnt lgkmcnt(4)
	v_mov_b32_e32 v8, v11
	v_mov_b32_e32 v9, v10
	s_waitcnt lgkmcnt(3)
	v_mov_b32_e32 v10, v13
	v_mov_b32_e32 v11, v12
	s_waitcnt lgkmcnt(2)
	v_mov_b32_e32 v12, v15
	v_mov_b32_e32 v13, v14
	s_waitcnt lgkmcnt(1)
	v_mov_b32_e32 v14, v21
	v_mov_b32_e32 v15, v20
	ds_read_b128 v[20:23], v113 offset:32
	v_subrev_u32_e32 v72, 44, v74
	s_waitcnt lgkmcnt(1)
	v_mfma_f32_32x32x16_bf16 v[0:15], v[16:19], v[92:95], v[0:15]
	v_add_u32_e32 v78, 0xffffff9c, v74
	v_add_u32_e32 v135, 0xffffff94, v74
	s_cmpk_lt_i32 s35, 0x1000
	s_cselect_b64 s[12:13], -1, 0
	s_cmpk_gt_i32 s35, 0xfff
	s_cselect_b64 s[10:11], -1, 0
	s_and_b64 vcc, exec, s[10:11]
	s_waitcnt lgkmcnt(0)
	v_mfma_f32_32x32x16_bf16 v[0:15], v[20:23], v[96:99], v[0:15]
	ds_read_b128 v[16:19], v113 offset:64
	ds_read_b128 v[20:23], v113 offset:96
	s_waitcnt lgkmcnt(1)
	v_mfma_f32_32x32x16_bf16 v[0:15], v[16:19], v[100:103], v[0:15]
	s_waitcnt lgkmcnt(0)
	v_mfma_f32_32x32x16_bf16 v[0:15], v[20:23], v[104:107], v[0:15]
	ds_read2_b32 v[18:19], v74 offset0:95 offset1:96
	ds_read2_b32 v[20:21], v74 offset0:93 offset1:94
	ds_read2_b32 v[22:23], v74 offset0:87 offset1:88
	ds_read2_b32 v[24:25], v74 offset0:85 offset1:86
	ds_read2_b32 v[26:27], v74 offset0:79 offset1:80
	ds_read2_b32 v[28:29], v74 offset0:77 offset1:78
	ds_read2_b32 v[30:31], v74 offset0:71 offset1:72
	ds_read2_b32 v[36:37], v74 offset0:69 offset1:70
	ds_read_b128 v[32:35], v113 offset:4608
	s_waitcnt lgkmcnt(8)
	v_mov_b32_e32 v16, v19
	v_mov_b32_e32 v17, v18
	s_waitcnt lgkmcnt(7)
	v_mov_b32_e32 v18, v21
	v_mov_b32_e32 v19, v20
	s_waitcnt lgkmcnt(6)
	v_mov_b32_e32 v20, v23
	v_mov_b32_e32 v21, v22
	s_waitcnt lgkmcnt(5)
	v_mov_b32_e32 v22, v25
	v_mov_b32_e32 v23, v24
	s_waitcnt lgkmcnt(4)
	v_mov_b32_e32 v24, v27
	v_mov_b32_e32 v25, v26
	s_waitcnt lgkmcnt(3)
	v_mov_b32_e32 v26, v29
	v_mov_b32_e32 v27, v28
	s_waitcnt lgkmcnt(2)
	v_mov_b32_e32 v28, v31
	v_mov_b32_e32 v29, v30
	s_waitcnt lgkmcnt(1)
	v_mov_b32_e32 v30, v37
	v_mov_b32_e32 v31, v36
	ds_read_b128 v[36:39], v113 offset:4640
	s_waitcnt lgkmcnt(1)
	v_mfma_f32_32x32x16_bf16 v[16:31], v[32:35], v[92:95], v[16:31]
	s_waitcnt lgkmcnt(0)
	v_mfma_f32_32x32x16_bf16 v[16:31], v[36:39], v[96:99], v[16:31]
	ds_read_b128 v[32:35], v113 offset:4672
	ds_read_b128 v[36:39], v113 offset:4704
	s_waitcnt lgkmcnt(1)
	v_mfma_f32_32x32x16_bf16 v[16:31], v[32:35], v[100:103], v[16:31]
	s_waitcnt lgkmcnt(0)
	v_mfma_f32_32x32x16_bf16 v[16:31], v[36:39], v[104:107], v[16:31]
	ds_read2_b32 v[34:35], v74 offset0:63 offset1:64
	ds_read2_b32 v[36:37], v74 offset0:61 offset1:62
	ds_read2_b32 v[38:39], v74 offset0:55 offset1:56
	ds_read2_b32 v[40:41], v74 offset0:53 offset1:54
	ds_read2_b32 v[42:43], v74 offset0:47 offset1:48
	ds_read2_b32 v[44:45], v74 offset0:45 offset1:46
	ds_read2_b32 v[46:47], v74 offset0:39 offset1:40
	ds_read2_b32 v[52:53], v74 offset0:37 offset1:38
	ds_read_b128 v[48:51], v113 offset:9216
	s_waitcnt lgkmcnt(8)
	v_mov_b32_e32 v32, v35
	v_mov_b32_e32 v33, v34
	s_waitcnt lgkmcnt(7)
	v_mov_b32_e32 v34, v37
	v_mov_b32_e32 v35, v36
	s_waitcnt lgkmcnt(6)
	v_mov_b32_e32 v36, v39
	v_mov_b32_e32 v37, v38
	s_waitcnt lgkmcnt(5)
	v_mov_b32_e32 v38, v41
	v_mov_b32_e32 v39, v40
	s_waitcnt lgkmcnt(4)
	v_mov_b32_e32 v40, v43
	v_mov_b32_e32 v41, v42
	s_waitcnt lgkmcnt(3)
	v_mov_b32_e32 v42, v45
	v_mov_b32_e32 v43, v44
	s_waitcnt lgkmcnt(2)
	v_mov_b32_e32 v44, v47
	v_mov_b32_e32 v45, v46
	s_waitcnt lgkmcnt(1)
	v_mov_b32_e32 v46, v53
	v_mov_b32_e32 v47, v52
	ds_read_b128 v[52:55], v113 offset:9248
	s_waitcnt lgkmcnt(1)
	v_mfma_f32_32x32x16_bf16 v[32:47], v[48:51], v[92:95], v[32:47]
	s_waitcnt lgkmcnt(0)
	v_mfma_f32_32x32x16_bf16 v[32:47], v[52:55], v[96:99], v[32:47]
	ds_read_b128 v[48:51], v113 offset:9280
	ds_read_b128 v[52:55], v113 offset:9312
	s_waitcnt lgkmcnt(1)
	v_mfma_f32_32x32x16_bf16 v[32:47], v[48:51], v[100:103], v[32:47]
	s_waitcnt lgkmcnt(0)
	v_mfma_f32_32x32x16_bf16 v[32:47], v[52:55], v[104:107], v[32:47]
	ds_read2_b32 v[50:51], v74 offset0:31 offset1:32
	ds_read2_b32 v[52:53], v74 offset0:29 offset1:30
	ds_read2_b32 v[54:55], v74 offset0:23 offset1:24
	ds_read2_b32 v[56:57], v74 offset0:21 offset1:22
	ds_read2_b32 v[58:59], v74 offset0:15 offset1:16
	ds_read2_b32 v[60:61], v74 offset0:13 offset1:14
	ds_read2_b32 v[62:63], v74 offset0:7 offset1:8
	ds_read2_b32 v[68:69], v74 offset0:5 offset1:6
	ds_read_b128 v[64:67], v113 offset:13824
	s_waitcnt lgkmcnt(8)
	v_mov_b32_e32 v48, v51
	v_mov_b32_e32 v49, v50
	s_waitcnt lgkmcnt(7)
	v_mov_b32_e32 v50, v53
	v_mov_b32_e32 v51, v52
	s_waitcnt lgkmcnt(6)
	v_mov_b32_e32 v52, v55
	v_mov_b32_e32 v53, v54
	s_waitcnt lgkmcnt(5)
	v_mov_b32_e32 v54, v57
	v_mov_b32_e32 v55, v56
	s_waitcnt lgkmcnt(4)
	v_mov_b32_e32 v56, v59
	v_mov_b32_e32 v57, v58
	s_waitcnt lgkmcnt(3)
	v_mov_b32_e32 v58, v61
	v_mov_b32_e32 v59, v60
	s_waitcnt lgkmcnt(2)
	v_mov_b32_e32 v60, v63
	v_mov_b32_e32 v61, v62
	s_waitcnt lgkmcnt(1)
	v_mov_b32_e32 v62, v69
	v_mov_b32_e32 v63, v68
	ds_read_b128 v[68:71], v113 offset:13856
	s_waitcnt lgkmcnt(1)
	v_mfma_f32_32x32x16_bf16 v[48:63], v[64:67], v[92:95], v[48:63]
	s_waitcnt lgkmcnt(0)
	v_mfma_f32_32x32x16_bf16 v[48:63], v[68:71], v[96:99], v[48:63]
	ds_read_b128 v[64:67], v113 offset:13888
	ds_read_b128 v[68:71], v113 offset:13920
	s_waitcnt lgkmcnt(1)
	v_mfma_f32_32x32x16_bf16 v[48:63], v[64:67], v[100:103], v[48:63]
	v_add_u32_e32 v64, -4, v74
	v_add_u32_e32 v65, -12, v74
	s_waitcnt lgkmcnt(0)
	v_mfma_f32_32x32x16_bf16 v[48:63], v[68:71], v[104:107], v[48:63]
	v_subrev_u32_e32 v70, 36, v74
	ds_read2_b32 v[66:67], v64 offset1:1
	ds_read2_b32 v[68:69], v65 offset1:1
	ds_read2_b32 v[70:71], v70 offset1:1
	ds_read2_b32 v[72:73], v72 offset1:1
	v_add_u32_e32 v64, 0xffffffbc, v74
	v_add_u32_e32 v65, 0xffffffb4, v74
	ds_read2_b32 v[74:75], v64 offset1:1
	ds_read2_b32 v[76:77], v65 offset1:1
	ds_read2_b32 v[78:79], v78 offset1:1
	ds_read2_b32 v[138:139], v135 offset1:1
	ds_read_b128 v[158:161], v113 offset:18432
	ds_read_b128 v[162:165], v113 offset:18464
	s_waitcnt lgkmcnt(9)
	v_mov_b32_e32 v64, v67
	v_mov_b32_e32 v65, v66
	s_waitcnt lgkmcnt(8)
	v_mov_b32_e32 v66, v69
	v_mov_b32_e32 v67, v68
	s_waitcnt lgkmcnt(7)
	v_mov_b32_e32 v68, v71
	v_mov_b32_e32 v69, v70
	s_waitcnt lgkmcnt(6)
	v_mov_b32_e32 v70, v73
	v_mov_b32_e32 v71, v72
	s_waitcnt lgkmcnt(5)
	v_mov_b32_e32 v72, v75
	v_mov_b32_e32 v73, v74
	s_waitcnt lgkmcnt(4)
	v_mov_b32_e32 v74, v77
	v_mov_b32_e32 v75, v76
	s_waitcnt lgkmcnt(3)
	v_mov_b32_e32 v76, v79
	v_mov_b32_e32 v77, v78
	s_waitcnt lgkmcnt(2)
	v_mov_b32_e32 v78, v139
	v_mov_b32_e32 v79, v138
	s_waitcnt lgkmcnt(1)
	s_nop 0
	v_mfma_f32_32x32x16_bf16 v[64:79], v[158:161], v[92:95], v[64:79]
	s_waitcnt lgkmcnt(0)
	v_mfma_f32_32x32x16_bf16 v[64:79], v[162:165], v[96:99], v[64:79]
	ds_read_b128 v[158:161], v113 offset:18496
	ds_read_b128 v[162:165], v113 offset:18528
	s_waitcnt lgkmcnt(1)
	v_mfma_f32_32x32x16_bf16 v[64:79], v[158:161], v[100:103], v[64:79]
	s_waitcnt lgkmcnt(0)
	v_mfma_f32_32x32x16_bf16 v[64:79], v[162:165], v[104:107], v[64:79]
	s_cbranch_vccnz .LBB0_885
	s_ashr_i32 s2, s35, 31
	s_lshr_b32 s3, s2, 23
	s_lshr_b32 s2, s2, 25
	s_add_i32 s2, s35, s2
	s_ashr_i32 s6, s2, 7
	s_add_i32 s3, s35, s3
	s_lshr_b32 s2, s6, 30
	s_ashr_i32 s14, s3, 9
	s_add_i32 s2, s6, s2
	s_lshl_b32 s9, s6, 13
	s_add_i32 s17, s23, s30
	s_and_b32 s2, s2, -4
	s_ashr_i32 s15, s14, 31
	s_sub_i32 s17, s17, s9
	s_sub_i32 s16, s6, s2
	s_lshl_b64 s[2:3], s[14:15], 13
	s_ashr_i32 s40, s17, 31
	s_add_u32 s2, s2, s17
	s_addc_u32 s3, s3, s40
	v_mov_b32_e32 v81, s3
	v_or_b32_e32 v80, s2, v122
	s_lshl_b32 s2, s16, 8
	v_lshlrev_b64 v[80:81], 11, v[80:81]
	s_or_b32 s2, s2, s26
	v_lshl_add_u64 v[80:81], s[4:5], 0, v[80:81]
	s_ashr_i32 s3, s2, 31
	v_lshl_add_u64 v[80:81], s[2:3], 1, v[80:81]
	v_mov_b32_e32 v135, v112
	v_lshl_add_u64 v[80:81], v[80:81], 0, v[134:135]
	global_load_dwordx4 v[92:95], v[80:81], off
	global_load_dwordx4 v[96:99], v[80:81], off offset:32
	global_load_dwordx4 v[100:103], v[80:81], off offset:64
	global_load_dwordx4 v[104:107], v[80:81], off offset:96
	s_lshl_b64 s[2:3], s[14:15], 22
	s_add_u32 s40, s18, s2
	s_addc_u32 s41, s19, s3
	s_lshl_b32 s16, s16, 6
	s_ashr_i32 s17, s16, 31
	s_lshl_b64 s[2:3], s[16:17], 1
	s_add_u32 s2, s40, s2
	s_addc_u32 s3, s41, s3
	v_mov_b32_e32 v137, v112
	v_lshl_add_u64 v[118:119], s[2:3], 0, v[136:137]
	s_sub_i32 s2, s30, s9
	v_mov_b32_e32 v113, v112
	v_add_u32_e32 v84, s2, v152
	v_mov_b32_e32 v114, v112
	v_mov_b32_e32 v115, v112
	v_mov_b64_e32 v[80:81], v[112:113]
	v_cmp_lt_i32_e32 vcc, -1, v84
	v_mov_b64_e32 v[82:83], v[114:115]
	s_and_saveexec_b64 s[2:3], vcc
	s_cbranch_execz .LBB0_872
	v_mov_b32_e32 v85, v112
	v_lshlrev_b64 v[80:81], 9, v[84:85]
	v_lshl_add_u64 v[80:81], v[118:119], 0, v[80:81]
	global_load_dwordx4 v[80:83], v[80:81], off
